# baseline (speedup 1.0000x reference)
.LBB1_4:
	s_or_b64 exec, exec, s[4:5]
	v_lshrrev_b32_e32 v6, 3, v0
	v_mul_u32_u24_e32 v4, 48, v0
	v_and_b32_e32 v6, 60, v6
	v_add3_u32 v4, v2, v4, v6
	s_waitcnt lgkmcnt(0)
	s_barrier
	ds_read_b32 v6, v4
	s_load_dwordx4 s[8:11], s[0:1], 0x40
	s_load_dwordx2 s[12:13], s[0:1], 0x28
	ds_read_b32 v2, v3
	v_lshlrev_b32_e64 v15, v0, 1
	s_lshl_b32 s3, s3, 3
	s_waitcnt lgkmcnt(0)
	v_bitop3_b32 v3, v6, v15, v6 bitop3:0x30
	ds_write_b32 v4, v3
	v_cmp_lt_i32_e32 vcc, -1, v2
	s_and_saveexec_b64 s[4:5], vcc
	v_lshlrev_b32_e64 v3, v2, 1
	v_lshrrev_b32_e32 v2, 3, v2
	v_and_b32_e32 v2, 0x1ffffffc, v2
	ds_or_b32 v2, v3 offset:34816
	s_or_b64 exec, exec, s[4:5]
	v_and_b32_e32 v3, 15, v0
	v_add_u32_e32 v8, s3, v1
	v_lshlrev_b32_e32 v4, 2, v3
	v_lshl_or_b32 v2, v8, 6, v4
	s_load_dwordx2 s[16:17], s[0:1], 0x20
	s_waitcnt lgkmcnt(0)
	s_barrier
	ds_read_b32 v6, v2
	s_lshl_b64 s[4:5], s[14:15], 9
	v_mov_b32_e32 v2, v8
	s_waitcnt lgkmcnt(0)
	s_branch .LBB1_8
	.p2align	6

.Lfarslow_ret_pre:
	v_pk_add_f32 v[120:121], v[120:121], v[128:129]
	v_pk_add_f32 v[122:123], v[122:123], v[130:131]
	v_pk_add_f32 v[120:121], v[120:121], v[140:141]
	v_pk_add_f32 v[122:123], v[122:123], v[142:143]
	s_nop 1
	v_permlane32_swap_b32_e32 v120, v122
	v_permlane32_swap_b32_e32 v121, v123
	v_pk_add_f32 v[176:177], v[120:121], v[122:123]
	v_add_u32_e32 v138, 0xfffffe00, v138
	v_add_u32_e32 v139, 0xfffffe00, v139
	v_add_u32_e32 v156, 0xfffffa00, v156
	v_lshl_add_u64 v[158:159], v[158:159], 0, s[2:3]
	s_mov_b32 s5, 15
	s_mov_b32 s5, 15
	.p2align	6
